# n2 = RMSNorm(h) phase: norm-gain vector loaded once before the row-pair loop instead of four serialized loads per iteration behind vmcnt(0) drains
# speedup vs baseline: 1.0039x; 1.0039x over previous
; __device__ __forceinline__ void norm_row_n2x2(const float* hrow0, const float* hrow1, const float* g, bf16* o0, bf16* o1, unsigned char* e0, unsigned char* e1, int lane) {
;     const f32x4* x0 = (const f32x4*)hrow0 + lane; const f32x4* x1 = (const f32x4*)hrow1 + lane; f32x4 v[2][4]; float s0 = 0.f, s1 = 0.f;
; #pragma unroll
;     for (int j = 0; j < 4; ++j) { v[0][j] = x0[64 * j]; v[1][j] = x1[64 * j]; }
; #pragma unroll
;     for (int j = 0; j < 4; ++j) { s0 += (v[0][j].x * v[0][j].x + v[0][j].y * v[0][j].y) + (v[0][j].z * v[0][j].z + v[0][j].w * v[0][j].w);
;                                   s1 += (v[1][j].x * v[1][j].x + v[1][j].y * v[1][j].y) + (v[1][j].z * v[1][j].z + v[1][j].w * v[1][j].w); }
;     const float r0 = 1.f / sqrtf(wave_sum(s0) * (1.f / D) + 1e-6f), r1 = 1.f / sqrtf(wave_sum(s1) * (1.f / D) + 1e-6f);
; #pragma unroll
;     for (int j = 0; j < 4; ++j) { const f32x4 gv = ((const f32x4*)g)[lane + 64 * j]; const f32x4 a = v[0][j] * r0 * gv, b = v[1][j] * r1 * gv;
;         *(v2u*)(o0 + 4 * (lane + 64 * j)) = (v2u){cvt_pk_bf16(a.x, a.y), cvt_pk_bf16(a.z, a.w)}; *(v2u*)(o1 + 4 * (lane + 64 * j)) = (v2u){cvt_pk_bf16(b.x, b.y), cvt_pk_bf16(b.z, b.w)};
;         { const f32x4 a8 = a * 16.f, b8 = b * 16.f; int wa = 0, wb = 0;
;           wa = __builtin_amdgcn_cvt_pk_fp8_f32(a8.x, a8.y, wa, false); wa = __builtin_amdgcn_cvt_pk_fp8_f32(a8.z, a8.w, wa, true); wb = __builtin_amdgcn_cvt_pk_fp8_f32(b8.x, b8.y, wb, false); wb = __builtin_amdgcn_cvt_pk_fp8_f32(b8.z, b8.w, wb, true);
;           *(unsigned*)(e0 + 4 * (lane + 64 * j)) = (unsigned)wa; *(unsigned*)(e1 + 4 * (lane + 64 * j)) = (unsigned)wb; } }
; }
; __global__ void __launch_bounds__(NWAVES * 64, 2) trunk_fwd(Args args) {
;     ...
;         for (int rep = 0; rep < REP_I; ++rep) {   if (rep) xcd_barrier(bar, F.wave0); phase_ids(F); const int gw = F.bx * NWAVES + F.wave, NGW = F.G * NWAVES; const float* g2 = args.in[3] + (size_t)layer * 1024;
;             for (int m = gw; m < T / 2; m += NGW) norm_row_n2x2(F.h + (size_t)m * D, F.h + (size_t)(m + T / 2) * D, g2, (bf16*)(ws + WS_N2) + (size_t)m * D, (bf16*)(ws + WS_N2) + (size_t)(m + T / 2) * D, (unsigned char*)(ws + WS_N8) + (size_t)m * D, (unsigned char*)(ws + WS_N8) + (size_t)(m + T / 2) * D, F.lane); }
.LBB0_1563:
	v_readlane_b32 s2, v253, 44
	v_readlane_b32 s3, v253, 45
	v_readlane_b32 s22, v255, 20
	s_mov_b64 s[0:1], s[6:7]
	s_mov_b64 s[18:19], s[6:7]
	s_and_b64 vcc, exec, s[2:3]
	v_readlane_b32 s23, v255, 21
	s_waitcnt lgkmcnt(0)
	s_barrier
	v_mbcnt_lo_u32_b32 v2, -1, 0
	v_mbcnt_hi_u32_b32 v2, -1, v2
	s_cbranch_vccz .LBB0_1566
	v_ashrrev_i32_e32 v3, 31, v2
	v_lshlrev_b64 v[34:35], 4, v[2:3]
	v_lshlrev_b32_e32 v2, 2, v2
	v_add_u32_e32 v4, 0x100, v2
	v_add_u32_e32 v6, 0x200, v2
	v_add_u32_e32 v8, 0x300, v2
	v_readlane_b32 s36, v251, 2
	v_ashrrev_i32_e32 v3, 31, v2
	v_ashrrev_i32_e32 v5, 31, v4
	v_ashrrev_i32_e32 v7, 31, v6
	v_ashrrev_i32_e32 v9, 31, v8
	v_readlane_b32 s6, v254, 52
	s_lshl_b64 s[2:3], s[60:61], 2
	v_readlane_b32 s42, v251, 8
	v_lshlrev_b64 v[10:11], 1, v[2:3]
	v_readlane_b32 s7, v254, 53
	v_lshlrev_b64 v[12:13], 1, v[4:5]
	v_lshlrev_b64 v[14:15], 1, v[6:7]
	v_lshlrev_b64 v[16:17], 1, v[8:9]
	v_readlane_b32 s43, v251, 9
	s_add_u32 s2, s42, s2
	v_lshl_add_u64 v[40:41], s[6:7], 0, v[10:11]
	v_lshl_add_u64 v[42:43], s[6:7], 0, v[12:13]
	v_lshl_add_u64 v[44:45], s[6:7], 0, v[14:15]
	v_lshl_add_u64 v[46:47], s[6:7], 0, v[16:17]
	v_readlane_b32 s6, v254, 56
	s_addc_u32 s3, s43, s3
	v_readlane_b32 s7, v254, 57
	v_lshl_add_u64 v[36:37], s[2:3], 0, v[34:35]
	v_readlane_b32 s2, v254, 48
	v_lshl_add_u64 v[48:49], s[6:7], 0, v[2:3]
	v_lshl_add_u64 v[50:51], s[6:7], 0, v[4:5]
	v_lshl_add_u64 v[52:53], s[6:7], 0, v[6:7]
	v_lshl_add_u64 v[54:55], s[6:7], 0, v[8:9]
	v_readlane_b32 s6, v254, 62
	v_readlane_b32 s3, v254, 49
	v_readlane_b32 s7, v254, 63
	v_readlane_b32 s20, v254, 60
	v_lshl_add_u64 v[38:39], s[2:3], 0, v[8:9]
	v_lshl_add_u64 v[56:57], s[2:3], 0, v[6:7]
	v_lshl_add_u64 v[58:59], s[6:7], 0, v[10:11]
	v_lshl_add_u64 v[60:61], s[6:7], 0, v[12:13]
	v_lshl_add_u64 v[62:63], s[6:7], 0, v[14:15]
	v_lshl_add_u64 v[64:65], s[6:7], 0, v[16:17]
	v_lshl_add_u64 v[66:67], s[2:3], 0, v[2:3]
	v_lshl_add_u64 v[68:69], s[2:3], 0, v[4:5]
	v_readlane_b32 s2, v254, 58
	v_readlane_b32 s6, v254, 50
	v_readlane_b32 s3, v254, 59
	v_readlane_b32 s7, v254, 51
	s_mov_b32 s5, s20
	v_readlane_b32 s37, v251, 3
	v_readlane_b32 s38, v251, 4
	v_readlane_b32 s39, v251, 5
	v_readlane_b32 s40, v251, 6
	v_readlane_b32 s41, v251, 7
	v_readlane_b32 s44, v251, 10
	v_readlane_b32 s45, v251, 11
	v_readlane_b32 s46, v251, 12
	v_readlane_b32 s47, v251, 13
	v_readlane_b32 s48, v251, 14
	v_readlane_b32 s49, v251, 15
	v_readlane_b32 s50, v251, 16
	v_readlane_b32 s51, v251, 17
	v_readlane_b32 s21, v254, 61
	global_load_dwordx4 v[100:103], v[36:37], off
	global_load_dwordx4 v[104:107], v[36:37], off offset:1024
	global_load_dwordx4 v[108:111], v[36:37], off offset:2048
	global_load_dwordx4 v[112:115], v[36:37], off offset:3072
	s_waitcnt vmcnt(0)
.LBB0_1565:
	v_lshl_add_u64 v[2:3], s[2:3], 0, v[34:35]
	v_lshl_add_u64 v[4:5], s[6:7], 0, v[34:35]
	global_load_dwordx4 v[30:33], v[2:3], off
	global_load_dwordx4 v[26:29], v[4:5], off
	global_load_dwordx4 v[22:25], v[2:3], off offset:1024
	global_load_dwordx4 v[18:21], v[4:5], off offset:1024
	global_load_dwordx4 v[14:17], v[2:3], off offset:2048
	global_load_dwordx4 v[10:13], v[4:5], off offset:2048
	global_load_dwordx4 v[6:9], v[2:3], off offset:3072
	s_nop 0
	global_load_dwordx4 v[2:5], v[4:5], off offset:3072
	s_add_i32 s5, s5, s82
	s_add_u32 s6, s6, s22
	s_addc_u32 s7, s7, s23
	s_add_u32 s2, s2, s22
	s_addc_u32 s3, s3, s23
	s_cmpk_gt_i32 s5, 0x3fff
	s_waitcnt vmcnt(7)
	v_mul_f32_e32 v1, v31, v31
	v_mul_f32_e32 v70, v33, v33
	v_fmac_f32_e32 v1, v30, v30
	v_fmac_f32_e32 v70, v32, v32
	v_add_f32_e32 v1, v1, v70
	s_waitcnt vmcnt(6)
	v_mul_f32_e32 v70, v27, v27
	v_mul_f32_e32 v71, v29, v29
	v_fmac_f32_e32 v70, v26, v26
	v_fmac_f32_e32 v71, v28, v28
	v_add_f32_e32 v70, v70, v71
	s_waitcnt vmcnt(5)
	v_mul_f32_e32 v71, v23, v23
	v_mul_f32_e32 v72, v25, v25
	v_fmac_f32_e32 v71, v22, v22
	v_fmac_f32_e32 v72, v24, v24
	v_add_f32_e32 v71, v71, v72
	v_add_f32_e32 v1, v1, v71
	s_waitcnt vmcnt(4)
	v_mul_f32_e32 v71, v19, v19
	v_mul_f32_e32 v72, v21, v21
	v_fmac_f32_e32 v71, v18, v18
	v_fmac_f32_e32 v72, v20, v20
	v_add_f32_e32 v71, v71, v72
	v_add_f32_e32 v70, v70, v71
	s_waitcnt vmcnt(3)
	v_mul_f32_e32 v71, v15, v15
	v_mul_f32_e32 v72, v17, v17
	v_fmac_f32_e32 v71, v14, v14
	v_fmac_f32_e32 v72, v16, v16
	v_add_f32_e32 v71, v71, v72
	v_add_f32_e32 v1, v1, v71
	s_waitcnt vmcnt(2)
	v_mul_f32_e32 v71, v11, v11
	v_mul_f32_e32 v72, v13, v13
	v_fmac_f32_e32 v71, v10, v10
	v_fmac_f32_e32 v72, v12, v12
	v_add_f32_e32 v71, v71, v72
	v_add_f32_e32 v70, v70, v71
	s_waitcnt vmcnt(1)
	v_mul_f32_e32 v71, v7, v7
	v_mul_f32_e32 v72, v9, v9
	v_fmac_f32_e32 v71, v6, v6
	v_fmac_f32_e32 v72, v8, v8
	v_add_f32_e32 v71, v71, v72
	v_add_f32_e32 v1, v1, v71
	s_waitcnt vmcnt(0)
; __device__ __forceinline__ unsigned cvt_pk_bf16(float lo, float hi) { unsigned r; asm volatile("v_cvt_pk_bf16_f32 %0, %1, %2" : "=v"(r) : "v"(lo), "v"(hi)); return r; }
; __device__ __forceinline__ void norm_row_n2x2(const float* hrow0, const float* hrow1, const float* g, bf16* o0, bf16* o1, unsigned char* e0, unsigned char* e1, int lane) {
;     ...
;     const float r0 = 1.f / sqrtf(wave_sum(s0) * (1.f / D) + 1e-6f), r1 = 1.f / sqrtf(wave_sum(s1) * (1.f / D) + 1e-6f);
; #pragma unroll
;     for (int j = 0; j < 4; ++j) { const f32x4 gv = ((const f32x4*)g)[lane + 64 * j]; const f32x4 a = v[0][j] * r0 * gv, b = v[1][j] * r1 * gv;
;         *(v2u*)(o0 + 4 * (lane + 64 * j)) = (v2u){cvt_pk_bf16(a.x, a.y), cvt_pk_bf16(a.z, a.w)}; *(v2u*)(o1 + 4 * (lane + 64 * j)) = (v2u){cvt_pk_bf16(b.x, b.y), cvt_pk_bf16(b.z, b.w)};
;         { const f32x4 a8 = a * 16.f, b8 = b * 16.f; int wa = 0, wb = 0;
;           wa = __builtin_amdgcn_cvt_pk_fp8_f32(a8.x, a8.y, wa, false); wa = __builtin_amdgcn_cvt_pk_fp8_f32(a8.z, a8.w, wa, true); wb = __builtin_amdgcn_cvt_pk_fp8_f32(b8.x, b8.y, wb, false); wb = __builtin_amdgcn_cvt_pk_fp8_f32(b8.z, b8.w, wb, true);
;           *(unsigned*)(e0 + 4 * (lane + 64 * j)) = (unsigned)wa; *(unsigned*)(e1 + 4 * (lane + 64 * j)) = (unsigned)wb; } }
	v_mul_f32_e32 v71, v3, v3
	v_mul_f32_e32 v72, v5, v5
	v_add_f32_dpp v1, v1, v1 quad_perm:[1,0,3,2] row_mask:0xf bank_mask:0xf bound_ctrl:1
	v_fmac_f32_e32 v71, v2, v2
	v_fmac_f32_e32 v72, v4, v4
	v_add_f32_dpp v1, v1, v1 quad_perm:[2,3,0,1] row_mask:0xf bank_mask:0xf bound_ctrl:1
	v_add_f32_e32 v71, v71, v72
	v_add_f32_e32 v71, v70, v71
	v_add_f32_dpp v1, v1, v1 row_half_mirror row_mask:0xf bank_mask:0xf bound_ctrl:1
	s_nop 1
	v_add_f32_dpp v1, v1, v1 row_mirror row_mask:0xf bank_mask:0xf bound_ctrl:1
	v_mov_b32_e32 v70, v1
	s_nop 1
	v_permlane16_swap_b32_e32 v1, v70
	v_add_f32_e32 v1, v1, v70
	v_mov_b32_e32 v70, v1
	s_nop 1
	v_permlane32_swap_b32_e32 v1, v70
	v_add_f32_e32 v1, v1, v70
	v_fmamk_f32 v1, v1, 0x3a800000, v244
	v_cmp_gt_f32_e32 vcc, s69, v1
	v_mul_f32_e32 v70, 0x4f800000, v1
	s_nop 0
	v_cndmask_b32_e32 v1, v1, v70, vcc
	v_sqrt_f32_e32 v70, v1
	s_nop 0
	v_add_u32_e32 v72, -1, v70
	v_fma_f32 v73, -v72, v70, v1
	v_cmp_ge_f32_e64 s[38:39], 0, v73
	v_add_u32_e32 v73, 1, v70
	s_nop 0
	v_cndmask_b32_e64 v72, v70, v72, s[38:39]
	v_fma_f32 v70, -v73, v70, v1
	v_cmp_lt_f32_e64 s[38:39], 0, v70
	s_nop 1
	v_cndmask_b32_e64 v70, v72, v73, s[38:39]
	v_mul_f32_e32 v72, 0x37800000, v70
	v_cndmask_b32_e32 v70, v70, v72, vcc
	v_cmp_class_f32_e32 vcc, v1, v242
	s_nop 1
	v_cndmask_b32_e32 v1, v70, v1, vcc
	v_div_scale_f32 v70, s[20:21], v1, v1, 1.0
	v_rcp_f32_e32 v72, v70
	s_nop 0
	v_fma_f32 v73, -v70, v72, 1.0
	v_fmac_f32_e32 v72, v73, v72
	v_div_scale_f32 v73, vcc, 1.0, v1, 1.0
	v_mul_f32_e32 v74, v73, v72
	v_fma_f32 v75, -v70, v74, v73
	v_fmac_f32_e32 v74, v75, v72
	v_fma_f32 v70, -v70, v74, v73
	v_div_fmas_f32 v70, v70, v72, v74
	v_div_fixup_f32 v70, v70, v1, 1.0
	v_add_f32_dpp v1, v71, v71 quad_perm:[1,0,3,2] row_mask:0xf bank_mask:0xf bound_ctrl:1
	s_nop 1
	v_add_f32_dpp v1, v1, v1 quad_perm:[2,3,0,1] row_mask:0xf bank_mask:0xf bound_ctrl:1
	s_nop 1
	v_add_f32_dpp v1, v1, v1 row_half_mirror row_mask:0xf bank_mask:0xf bound_ctrl:1
	s_nop 1
	v_add_f32_dpp v1, v1, v1 row_mirror row_mask:0xf bank_mask:0xf bound_ctrl:1
	v_mov_b32_e32 v71, v1
	s_nop 1
	v_permlane16_swap_b32_e32 v1, v71
	v_add_f32_e32 v1, v1, v71
	v_mov_b32_e32 v71, v1
	s_nop 1
	v_permlane32_swap_b32_e32 v1, v71
	v_add_f32_e32 v1, v1, v71
	v_fmamk_f32 v1, v1, 0x3a800000, v244
	v_cmp_gt_f32_e32 vcc, s69, v1
	v_mul_f32_e32 v71, 0x4f800000, v1
	s_nop 0
	v_cndmask_b32_e32 v1, v1, v71, vcc
	v_sqrt_f32_e32 v71, v1
	s_nop 0
	v_add_u32_e32 v72, -1, v71
	v_fma_f32 v73, -v72, v71, v1
	v_cmp_ge_f32_e64 s[38:39], 0, v73
	v_add_u32_e32 v73, 1, v71
	s_nop 0
	v_cndmask_b32_e64 v72, v71, v72, s[38:39]
	v_fma_f32 v71, -v73, v71, v1
	v_cmp_lt_f32_e64 s[38:39], 0, v71
	s_nop 1
	v_cndmask_b32_e64 v71, v72, v73, s[38:39]
	v_mul_f32_e32 v72, 0x37800000, v71
	v_cndmask_b32_e32 v71, v71, v72, vcc
	v_cmp_class_f32_e32 vcc, v1, v242
	s_nop 1
	v_cndmask_b32_e32 v1, v71, v1, vcc
	v_div_scale_f32 v71, s[20:21], v1, v1, 1.0
	v_rcp_f32_e32 v72, v71
	s_nop 0
	v_fma_f32 v73, -v71, v72, 1.0
	v_fmac_f32_e32 v72, v73, v72
	v_div_scale_f32 v73, vcc, 1.0, v1, 1.0
	v_mul_f32_e32 v74, v73, v72
	v_fma_f32 v75, -v71, v74, v73
	v_fmac_f32_e32 v74, v75, v72
	v_fma_f32 v71, -v71, v74, v73
	v_div_fmas_f32 v71, v71, v72, v74
	v_mov_b64_e32 v[74:75], v[100:101]
	v_mov_b64_e32 v[76:77], v[102:103]
	v_div_fixup_f32 v72, v71, v1, 1.0
	v_pk_mul_f32 v[30:31], v[30:31], v[70:71] op_sel_hi:[1,0]
	v_pk_mul_f32 v[32:33], v[32:33], v[70:71] op_sel_hi:[1,0]
	v_pk_mul_f32 v[26:27], v[26:27], v[72:73] op_sel_hi:[1,0]
	v_pk_mul_f32 v[28:29], v[28:29], v[72:73] op_sel_hi:[1,0]
	v_mov_b32_e32 v71, v0
	v_mov_b32_e32 v1, v0
	v_pk_mul_f32 v[18:19], v[18:19], v[72:73] op_sel_hi:[1,0]
	v_pk_mul_f32 v[20:21], v[20:21], v[72:73] op_sel_hi:[1,0]
	v_pk_mul_f32 v[10:11], v[10:11], v[72:73] op_sel_hi:[1,0]
	v_pk_mul_f32 v[12:13], v[12:13], v[72:73] op_sel_hi:[1,0]
	v_pk_mul_f32 v[2:3], v[2:3], v[72:73] op_sel_hi:[1,0]
	v_pk_mul_f32 v[4:5], v[4:5], v[72:73] op_sel_hi:[1,0]
	v_pk_mul_f32 v[30:31], v[74:75], v[30:31]
	v_pk_mul_f32 v[32:33], v[76:77], v[32:33]
	v_pk_mul_f32 v[28:29], v[76:77], v[28:29]
	v_pk_mul_f32 v[26:27], v[74:75], v[26:27]
	v_cvt_pk_bf16_f32 v74, v30, v31
	v_lshl_add_u64 v[76:77], s[0:1], 0, v[58:59]
	v_pk_mul_f32 v[30:31], v[30:31], s[10:11] op_sel_hi:[1,0]
	v_cvt_pk_bf16_f32 v75, v32, v33
	global_store_dwordx2 v[76:77], v[74:75], off
	v_cvt_pk_bf16_f32 v74, v26, v27
	v_pk_mul_f32 v[26:27], v[26:27], s[10:11] op_sel_hi:[1,0]
	v_cvt_pk_fp8_f32 v71, v30, v31
	v_cvt_pk_fp8_f32 v1, v26, v27
	v_pk_mul_f32 v[32:33], v[32:33], s[10:11] op_sel_hi:[1,0]
	v_cvt_pk_bf16_f32 v75, v28, v29
	v_pk_mul_f32 v[28:29], v[28:29], s[10:11] op_sel_hi:[1,0]
	v_cvt_pk_fp8_f32 v71, v32, v33 op_sel:[0,0,1]
	v_cvt_pk_fp8_f32 v1, v28, v29 op_sel:[0,0,1]
	v_lshl_add_u64 v[76:77], s[0:1], 0, v[40:41]
; __device__ __forceinline__ unsigned cvt_pk_bf16(float lo, float hi) { unsigned r; asm volatile("v_cvt_pk_bf16_f32 %0, %1, %2" : "=v"(r) : "v"(lo), "v"(hi)); return r; }
; __device__ __forceinline__ void norm_row_n2x2(const float* hrow0, const float* hrow1, const float* g, bf16* o0, bf16* o1, unsigned char* e0, unsigned char* e1, int lane) {
;     ...
;     for (int j = 0; j < 4; ++j) { const f32x4 gv = ((const f32x4*)g)[lane + 64 * j]; const f32x4 a = v[0][j] * r0 * gv, b = v[1][j] * r1 * gv;
;         *(v2u*)(o0 + 4 * (lane + 64 * j)) = (v2u){cvt_pk_bf16(a.x, a.y), cvt_pk_bf16(a.z, a.w)}; *(v2u*)(o1 + 4 * (lane + 64 * j)) = (v2u){cvt_pk_bf16(b.x, b.y), cvt_pk_bf16(b.z, b.w)};
;         { const f32x4 a8 = a * 16.f, b8 = b * 16.f; int wa = 0, wb = 0;
;           wa = __builtin_amdgcn_cvt_pk_fp8_f32(a8.x, a8.y, wa, false); wa = __builtin_amdgcn_cvt_pk_fp8_f32(a8.z, a8.w, wa, true); wb = __builtin_amdgcn_cvt_pk_fp8_f32(b8.x, b8.y, wb, false); wb = __builtin_amdgcn_cvt_pk_fp8_f32(b8.z, b8.w, wb, true);
;           *(unsigned*)(e0 + 4 * (lane + 64 * j)) = (unsigned)wa; *(unsigned*)(e1 + 4 * (lane + 64 * j)) = (unsigned)wb; } }
	v_lshl_add_u64 v[26:27], s[0:1], 0, v[66:67]
	global_store_dwordx2 v[76:77], v[74:75], off
	global_store_dword v[26:27], v71, off
	v_lshl_add_u64 v[26:27], s[0:1], 0, v[48:49]
	global_store_dword v[26:27], v1, off
	v_mov_b64_e32 v[26:27], v[104:105]
	v_mov_b64_e32 v[28:29], v[106:107]
	v_pk_mul_f32 v[22:23], v[22:23], v[70:71] op_sel_hi:[1,0]
	v_pk_mul_f32 v[24:25], v[24:25], v[70:71] op_sel_hi:[1,0]
	v_mov_b32_e32 v1, v0
	v_pk_mul_f32 v[14:15], v[14:15], v[70:71] op_sel_hi:[1,0]
	v_pk_mul_f32 v[16:17], v[16:17], v[70:71] op_sel_hi:[1,0]
	v_pk_mul_f32 v[6:7], v[6:7], v[70:71] op_sel_hi:[1,0]
	v_pk_mul_f32 v[8:9], v[8:9], v[70:71] op_sel_hi:[1,0]
	v_lshl_add_u64 v[40:41], v[40:41], 0, s[54:55]
	v_lshl_add_u64 v[48:49], v[48:49], 0, s[96:97]
	v_lshl_add_u64 v[58:59], v[58:59], 0, s[54:55]
	v_lshl_add_u64 v[66:67], v[66:67], 0, s[96:97]
	v_pk_mul_f32 v[22:23], v[22:23], v[26:27]
	v_pk_mul_f32 v[24:25], v[24:25], v[28:29]
	v_pk_mul_f32 v[20:21], v[20:21], v[28:29]
	v_pk_mul_f32 v[18:19], v[18:19], v[26:27]
	v_cvt_pk_bf16_f32 v26, v22, v23
	v_lshl_add_u64 v[28:29], s[0:1], 0, v[60:61]
	v_pk_mul_f32 v[22:23], v[22:23], s[10:11] op_sel_hi:[1,0]
	v_cvt_pk_bf16_f32 v27, v24, v25
	global_store_dwordx2 v[28:29], v[26:27], off
	v_cvt_pk_bf16_f32 v26, v18, v19
	v_pk_mul_f32 v[18:19], v[18:19], s[10:11] op_sel_hi:[1,0]
	v_cvt_pk_fp8_f32 v1, v22, v23
	v_mov_b32_e32 v22, v0
	v_cvt_pk_fp8_f32 v22, v18, v19
	v_pk_mul_f32 v[24:25], v[24:25], s[10:11] op_sel_hi:[1,0]
	v_cvt_pk_bf16_f32 v27, v20, v21
	v_pk_mul_f32 v[20:21], v[20:21], s[10:11] op_sel_hi:[1,0]
	v_cvt_pk_fp8_f32 v1, v24, v25 op_sel:[0,0,1]
	v_cvt_pk_fp8_f32 v22, v20, v21 op_sel:[0,0,1]
	v_lshl_add_u64 v[28:29], s[0:1], 0, v[42:43]
	v_lshl_add_u64 v[18:19], s[0:1], 0, v[68:69]
	global_store_dwordx2 v[28:29], v[26:27], off
	global_store_dword v[18:19], v1, off
	v_lshl_add_u64 v[18:19], s[0:1], 0, v[50:51]
	global_store_dword v[18:19], v22, off
	v_mov_b64_e32 v[18:19], v[108:109]
	v_mov_b64_e32 v[20:21], v[110:111]
	v_mov_b32_e32 v1, v0
	v_lshl_add_u64 v[42:43], v[42:43], 0, s[54:55]
	v_lshl_add_u64 v[50:51], v[50:51], 0, s[96:97]
	v_lshl_add_u64 v[60:61], v[60:61], 0, s[54:55]
	v_lshl_add_u64 v[68:69], v[68:69], 0, s[96:97]
	v_pk_mul_f32 v[14:15], v[14:15], v[18:19]
	v_pk_mul_f32 v[16:17], v[16:17], v[20:21]
	v_pk_mul_f32 v[12:13], v[12:13], v[20:21]
	v_pk_mul_f32 v[10:11], v[10:11], v[18:19]
	v_cvt_pk_bf16_f32 v18, v14, v15
	v_lshl_add_u64 v[20:21], s[0:1], 0, v[62:63]
	v_pk_mul_f32 v[14:15], v[14:15], s[10:11] op_sel_hi:[1,0]
	v_cvt_pk_bf16_f32 v19, v16, v17
	global_store_dwordx2 v[20:21], v[18:19], off
	v_cvt_pk_bf16_f32 v18, v10, v11
	v_pk_mul_f32 v[10:11], v[10:11], s[10:11] op_sel_hi:[1,0]
	v_cvt_pk_fp8_f32 v1, v14, v15
	v_mov_b32_e32 v14, v0
	v_cvt_pk_fp8_f32 v14, v10, v11
	v_pk_mul_f32 v[16:17], v[16:17], s[10:11] op_sel_hi:[1,0]
	v_cvt_pk_bf16_f32 v19, v12, v13
	v_pk_mul_f32 v[12:13], v[12:13], s[10:11] op_sel_hi:[1,0]
	v_cvt_pk_fp8_f32 v1, v16, v17 op_sel:[0,0,1]
	v_cvt_pk_fp8_f32 v14, v12, v13 op_sel:[0,0,1]
	v_lshl_add_u64 v[20:21], s[0:1], 0, v[44:45]
	v_lshl_add_u64 v[10:11], s[0:1], 0, v[56:57]
	global_store_dwordx2 v[20:21], v[18:19], off
	global_store_dword v[10:11], v1, off
	v_lshl_add_u64 v[10:11], s[0:1], 0, v[52:53]
	global_store_dword v[10:11], v14, off
	v_mov_b64_e32 v[10:11], v[112:113]
	v_mov_b64_e32 v[12:13], v[114:115]
	v_mov_b32_e32 v1, v0
	v_lshl_add_u64 v[44:45], v[44:45], 0, s[54:55]
	v_lshl_add_u64 v[52:53], v[52:53], 0, s[96:97]
	v_lshl_add_u64 v[56:57], v[56:57], 0, s[96:97]
	v_lshl_add_u64 v[62:63], v[62:63], 0, s[54:55]
	v_pk_mul_f32 v[6:7], v[6:7], v[10:11]
	v_pk_mul_f32 v[8:9], v[8:9], v[12:13]
	v_pk_mul_f32 v[4:5], v[4:5], v[12:13]
	v_pk_mul_f32 v[2:3], v[2:3], v[10:11]
	v_cvt_pk_bf16_f32 v10, v6, v7
	v_lshl_add_u64 v[12:13], s[0:1], 0, v[64:65]
	v_pk_mul_f32 v[6:7], v[6:7], s[10:11] op_sel_hi:[1,0]
	v_cvt_pk_bf16_f32 v11, v8, v9
	global_store_dwordx2 v[12:13], v[10:11], off
	v_cvt_pk_bf16_f32 v10, v2, v3
	v_pk_mul_f32 v[2:3], v[2:3], s[10:11] op_sel_hi:[1,0]
	v_cvt_pk_fp8_f32 v1, v6, v7
	v_mov_b32_e32 v6, v0
	v_cvt_pk_fp8_f32 v6, v2, v3
	v_pk_mul_f32 v[8:9], v[8:9], s[10:11] op_sel_hi:[1,0]
	v_cvt_pk_bf16_f32 v11, v4, v5
	v_pk_mul_f32 v[4:5], v[4:5], s[10:11] op_sel_hi:[1,0]
	v_cvt_pk_fp8_f32 v1, v8, v9 op_sel:[0,0,1]
	v_cvt_pk_fp8_f32 v6, v4, v5 op_sel:[0,0,1]
	v_lshl_add_u64 v[12:13], s[0:1], 0, v[46:47]
	v_lshl_add_u64 v[2:3], s[0:1], 0, v[38:39]
	global_store_dwordx2 v[12:13], v[10:11], off
	global_store_dword v[2:3], v1, off
	v_lshl_add_u64 v[2:3], s[0:1], 0, v[54:55]
	v_lshl_add_u64 v[38:39], v[38:39], 0, s[96:97]
	v_lshl_add_u64 v[46:47], v[46:47], 0, s[54:55]
	v_lshl_add_u64 v[54:55], v[54:55], 0, s[96:97]
	v_lshl_add_u64 v[64:65], v[64:65], 0, s[54:55]
	global_store_dword v[2:3], v6, off
	s_cbranch_scc0 .LBB0_1565
